# baseline (speedup 1.0000x reference)
_Z16sum_layer_kernelPKfS0_Pf:
	s_load_dwordx4 s[4:7], s[0:1], 0x0
	s_load_dwordx2 s[8:9], s[0:1], 0x10
	v_and_b32_e32 v40, 31, v0
	v_bfe_u32 v41, v0, 5, 1
	v_lshrrev_b32_e32 v42, 6, v0
	v_and_b32_e32 v43, 7, v0
	v_bfe_u32 v44, v0, 3, 3
	v_and_b32_e32 v45, 63, v0
	s_lshl_b32 s3, s2, 12
	s_lshl_b32 s19, s2, 7
	v_lshlrev_b32_e32 v1, 11, v41
	v_lshl_or_b32 v1, v40, 2, v1
	v_lshlrev_b32_e32 v46, 4, v43
	v_lshl_add_u32 v35, v44, 16, v46
	v_lshl_add_u32 v35, v42, 21, v35
	v_add_u32_e32 v35, s19, v35
	v_lshlrev_b32_e32 v36, 2, v40
	v_lshl_add_u32 v36, v41, 18, v36
	v_lshl_add_u32 v36, v42, 21, v36
	v_add_u32_e32 v36, s19, v36
	v_mul_u32_u24_e32 v37, 0x1200, v42
	v_mul_u32_u24_e32 v38, 0x90, v44
	v_add3_u32 v38, v37, v38, v46
	v_mul_u32_u24_e32 v39, 0x90, v40
	v_lshlrev_b32_e32 v47, 6, v41
	v_add3_u32 v39, v37, v39, v47
	v_cmp_gt_u32_e32 vcc, 32, v45
	v_mov_b32_e32 v48, 0xc1600000
	s_mov_b32 s16, 0x3fb8aa3b
	s_mov_b32 s17, 0x3f317218
	s_mov_b32 s20, 0x80000
	s_mov_b32 s21, 0x100000
	s_mov_b32 s22, 0x180000
	s_lshl_b32 s24, 1, 16
	s_lshl_b32 s25, 2, 16
	s_lshl_b32 s26, 3, 16
	s_lshl_b32 s27, 8, 16
	s_lshl_b32 s28, 9, 16
	s_lshl_b32 s29, 10, 16
	s_lshl_b32 s30, 11, 16
	s_lshl_b32 s31, 16, 16
	s_lshl_b32 s32, 17, 16
	s_lshl_b32 s33, 18, 16
	s_lshl_b32 s34, 19, 16
	s_lshl_b32 s35, 24, 16
	s_lshl_b32 s36, 25, 16
	s_lshl_b32 s37, 26, 16
	s_lshl_b32 s38, 27, 16
	s_mov_b32 s14, 0x200000
	s_mov_b32 s15, 0x20000
	s_waitcnt lgkmcnt(0)
	s_mov_b32 s12, s6
	s_and_b32 s13, s7, 0xffff
	s_and_b32 s5, s5, 0xffff
	s_mov_b32 s6, 0x800000
	s_mov_b32 s7, s15
	s_and_b32 s9, s9, 0xffff
	s_mov_b32 s10, s6
	s_mov_b32 s11, s15
	buffer_load_dword v18, v1, s[12:15], s3 offen nt
	buffer_load_dword v19, v1, s[12:15], s3 offen offset:128 nt
	buffer_load_dword v20, v1, s[12:15], s3 offen offset:256 nt
	buffer_load_dword v21, v1, s[12:15], s3 offen offset:384 nt
	buffer_load_dword v22, v1, s[12:15], s3 offen offset:512 nt
	buffer_load_dword v23, v1, s[12:15], s3 offen offset:640 nt
	buffer_load_dword v24, v1, s[12:15], s3 offen offset:768 nt
	buffer_load_dword v25, v1, s[12:15], s3 offen offset:896 nt
	buffer_load_dword v26, v1, s[12:15], s3 offen offset:1024 nt
	buffer_load_dword v27, v1, s[12:15], s3 offen offset:1152 nt
	buffer_load_dword v28, v1, s[12:15], s3 offen offset:1280 nt
	buffer_load_dword v29, v1, s[12:15], s3 offen offset:1408 nt
	buffer_load_dword v30, v1, s[12:15], s3 offen offset:1536 nt
	buffer_load_dword v31, v1, s[12:15], s3 offen offset:1664 nt
	buffer_load_dword v32, v1, s[12:15], s3 offen offset:1792 nt
	buffer_load_dword v33, v1, s[12:15], s3 offen offset:1920 nt
	buffer_load_dwordx4 v[2:5], v35, s[4:7], 0 offen nt
	buffer_load_dwordx4 v[6:9], v35, s[4:7], s20 offen nt
	buffer_load_dwordx4 v[10:13], v35, s[4:7], s21 offen nt
	buffer_load_dwordx4 v[14:17], v35, s[4:7], s22 offen nt
	buffer_load_dword v34, v36, s[8:11], 0 offen nt
	s_waitcnt vmcnt(5)
	v_max3_f32 v49, v18, v19, v20
	v_max3_f32 v50, v21, v22, v23
	v_max3_f32 v49, v49, v24, v25
	v_max3_f32 v50, v50, v26, v27
	v_max3_f32 v49, v49, v28, v29
	v_max3_f32 v50, v50, v30, v31
	v_max3_f32 v49, v49, v32, v33
	v_max_f32_e32 v49, v49, v50
	v_mov_b32_e32 v50, v49
	s_nop 1
	v_permlane32_swap_b32_e32 v49, v50
	v_max_f32_e32 v49, v49, v50
	v_fmamk_f32 v49, v49, 0x3fb8aa3b, v48
	v_fma_f32 v18, v18, s16, -v49
	v_exp_f32_e32 v18, v18
	v_fma_f32 v19, v19, s16, -v49
	v_exp_f32_e32 v19, v19
	v_fma_f32 v20, v20, s16, -v49
	v_exp_f32_e32 v20, v20
	v_fma_f32 v21, v21, s16, -v49
	v_exp_f32_e32 v21, v21
	v_fma_f32 v22, v22, s16, -v49
	v_exp_f32_e32 v22, v22
	v_fma_f32 v23, v23, s16, -v49
	v_exp_f32_e32 v23, v23
	v_fma_f32 v24, v24, s16, -v49
	v_exp_f32_e32 v24, v24
	v_fma_f32 v25, v25, s16, -v49
	v_exp_f32_e32 v25, v25
	v_fma_f32 v26, v26, s16, -v49
	v_exp_f32_e32 v26, v26
	v_fma_f32 v27, v27, s16, -v49
	v_exp_f32_e32 v27, v27
	v_fma_f32 v28, v28, s16, -v49
	v_exp_f32_e32 v28, v28
	v_fma_f32 v29, v29, s16, -v49
	v_exp_f32_e32 v29, v29
	v_fma_f32 v30, v30, s16, -v49
	v_exp_f32_e32 v30, v30
	v_fma_f32 v31, v31, s16, -v49
	v_exp_f32_e32 v31, v31
	v_fma_f32 v32, v32, s16, -v49
	v_exp_f32_e32 v32, v32
	v_fma_f32 v33, v33, s16, -v49
	v_exp_f32_e32 v33, v33
	v_add_f32_e32 v50, v18, v19
	v_add_f32_e32 v51, v20, v21
	v_add_f32_e32 v50, v50, v22
	v_add_f32_e32 v51, v51, v23
	v_add_f32_e32 v50, v50, v24
	v_add_f32_e32 v51, v51, v25
	v_add_f32_e32 v50, v50, v26
	v_add_f32_e32 v51, v51, v27
	v_add_f32_e32 v50, v50, v28
	v_add_f32_e32 v51, v51, v29
	v_add_f32_e32 v50, v50, v30
	v_add_f32_e32 v51, v51, v31
	v_add_f32_e32 v50, v50, v32
	v_add_f32_e32 v51, v51, v33
	v_add_f32_e32 v50, v50, v51
	v_mov_b32_e32 v51, v50
	s_nop 1
	v_permlane32_swap_b32_e32 v50, v51
	v_add_f32_e32 v50, v50, v51
	v_log_f32_e32 v50, v50
	v_cvt_pk_f16_f32 v52, v18, v19
	v_cvt_pk_f16_f32 v53, v20, v21
	v_cvt_pk_f16_f32 v54, v22, v23
	v_cvt_pk_f16_f32 v55, v24, v25
	v_cvt_pk_f16_f32 v56, v26, v27
	v_cvt_pk_f16_f32 v57, v28, v29
	v_cvt_pk_f16_f32 v58, v30, v31
	v_cvt_pk_f16_f32 v59, v32, v33
	v_add_f32_e32 v50, 0x41600000, v50
	v_mul_f32_e32 v50, 0xbf317218, v50
	v_cndmask_b32_e64 v51, v50, 1.0, vcc
	s_waitcnt vmcnt(4)
	ds_write_b128 v38, v[2:5]
	s_waitcnt vmcnt(3)
	ds_write_b128 v38, v[6:9] offset:1152
	s_waitcnt vmcnt(2)
	ds_write_b128 v38, v[10:13] offset:2304
	s_waitcnt vmcnt(1)
	ds_write_b128 v38, v[14:17] offset:3456
	ds_read_b128 v[60:63], v39
	ds_read_b128 v[64:67], v39 offset:16
	ds_read_b128 v[68:71], v39 offset:32
	ds_read_b128 v[72:75], v39 offset:48
	s_waitcnt lgkmcnt(2)
	v_max3_f32 v76, v60, v61, v62
	v_max3_f32 v77, v63, v64, v65
	v_max_f32_e32 v76, v76, v66
	v_max_f32_e32 v77, v77, v67
	s_waitcnt lgkmcnt(0)
	v_max3_f32 v76, v76, v68, v69
	v_max3_f32 v77, v77, v70, v71
	v_max3_f32 v76, v76, v72, v73
	v_max3_f32 v77, v77, v74, v75
	v_max_f32_e32 v76, v76, v77
	v_mov_b32_e32 v77, v76
	s_nop 1
	v_permlane32_swap_b32_e32 v76, v77
	v_max_f32_e32 v76, v76, v77
	v_cndmask_b32_e32 v78, 1.0, v76, vcc
	v_fmamk_f32 v79, v76, 0x3fb8aa3b, v48
	v_fma_f32 v60, v60, s16, -v79
	v_mfma_f32_32x32x2_f32 v[80:95], v78, v51, 0
	v_exp_f32_e32 v60, v60
	v_fma_f32 v61, v61, s16, -v79
	v_exp_f32_e32 v61, v61
	v_fma_f32 v62, v62, s16, -v79
	v_exp_f32_e32 v62, v62
	v_fma_f32 v63, v63, s16, -v79
	v_exp_f32_e32 v63, v63
	v_fma_f32 v64, v64, s16, -v79
	v_exp_f32_e32 v64, v64
	v_fma_f32 v65, v65, s16, -v79
	v_exp_f32_e32 v65, v65
	v_fma_f32 v66, v66, s16, -v79
	v_exp_f32_e32 v66, v66
	v_fma_f32 v67, v67, s16, -v79
	v_exp_f32_e32 v67, v67
	v_fma_f32 v68, v68, s16, -v79
	v_exp_f32_e32 v68, v68
	v_cvt_pk_f16_f32 v96, v60, v61
	v_cvt_pk_f16_f32 v97, v62, v63
	v_cvt_pk_f16_f32 v98, v64, v65
	v_cvt_pk_f16_f32 v99, v66, v67
	v_fma_f32 v69, v69, s16, -v79
	v_exp_f32_e32 v69, v69
	v_fma_f32 v70, v70, s16, -v79
	v_exp_f32_e32 v70, v70
	v_mfma_f32_32x32x16_f16 v[104:119], v[96:99], v[52:55], 0
	v_fma_f32 v71, v71, s16, -v79
	v_exp_f32_e32 v71, v71
	v_fma_f32 v72, v72, s16, -v79
	v_exp_f32_e32 v72, v72
	v_fma_f32 v73, v73, s16, -v79
	v_exp_f32_e32 v73, v73
	v_fma_f32 v74, v74, s16, -v79
	v_exp_f32_e32 v74, v74
	v_fma_f32 v75, v75, s16, -v79
	v_exp_f32_e32 v75, v75
	v_cvt_pk_f16_f32 v100, v68, v69
	v_cvt_pk_f16_f32 v101, v70, v71
	v_cvt_pk_f16_f32 v102, v72, v73
	v_cvt_pk_f16_f32 v103, v74, v75
	s_nop 1
	v_mfma_f32_32x32x16_f16 v[104:119], v[100:103], v[56:59], v[104:119]
	s_nop 11
	v_log_f32_e32 v104, v104
	v_log_f32_e32 v105, v105
	v_log_f32_e32 v106, v106
	v_fmac_f32_e32 v80, s17, v104
	buffer_store_dword v80, v36, s[8:11], 0 offen
	v_log_f32_e32 v107, v107
	v_fmac_f32_e32 v81, s17, v105
	buffer_store_dword v81, v36, s[8:11], s24 offen
	v_log_f32_e32 v108, v108
	v_fmac_f32_e32 v82, s17, v106
	buffer_store_dword v82, v36, s[8:11], s25 offen
	v_log_f32_e32 v109, v109
	v_fmac_f32_e32 v83, s17, v107
	buffer_store_dword v83, v36, s[8:11], s26 offen
	v_log_f32_e32 v110, v110
	v_fmac_f32_e32 v84, s17, v108
	buffer_store_dword v84, v36, s[8:11], s27 offen
	v_log_f32_e32 v111, v111
	v_fmac_f32_e32 v85, s17, v109
	buffer_store_dword v85, v36, s[8:11], s28 offen
	v_log_f32_e32 v112, v112
	v_fmac_f32_e32 v86, s17, v110
	buffer_store_dword v86, v36, s[8:11], s29 offen
	v_log_f32_e32 v113, v113
	v_fmac_f32_e32 v87, s17, v111
	buffer_store_dword v87, v36, s[8:11], s30 offen
	v_log_f32_e32 v114, v114
	v_fmac_f32_e32 v88, s17, v112
	buffer_store_dword v88, v36, s[8:11], s31 offen
	v_log_f32_e32 v115, v115
	v_fmac_f32_e32 v89, s17, v113
	buffer_store_dword v89, v36, s[8:11], s32 offen
	v_log_f32_e32 v116, v116
	v_fmac_f32_e32 v90, s17, v114
	buffer_store_dword v90, v36, s[8:11], s33 offen
	v_log_f32_e32 v117, v117
	v_fmac_f32_e32 v91, s17, v115
	buffer_store_dword v91, v36, s[8:11], s34 offen
	v_log_f32_e32 v118, v118
	v_fmac_f32_e32 v92, s17, v116
	buffer_store_dword v92, v36, s[8:11], s35 offen
	v_log_f32_e32 v119, v119
	v_fmac_f32_e32 v93, s17, v117
	buffer_store_dword v93, v36, s[8:11], s36 offen
	v_fmac_f32_e32 v94, s17, v118
	buffer_store_dword v94, v36, s[8:11], s37 offen
	v_fmac_f32_e32 v95, s17, v119
	buffer_store_dword v95, v36, s[8:11], s38 offen
	s_endpgm
